# P4 RG gate GEMM: epilogue's first five loads requested at the unit start (land under the K-loop), vmcnt(0) drain removed, the other seven conv-row loads issued before the gate math
# baseline (speedup 1.0000x reference)
.LBB0_635:
	s_andn2_b64 vcc, exec, s[20:21]
	s_cbranch_vccnz .Lzs_3
	s_add_i32 s28, s79, 0x80
	s_add_i32 s79, s75, 0x100
	s_mov_b32 s80, 0
	s_and_b32 s98, s12, 1
	s_lshl_b32 s99, s12, 6
	s_and_b32 s99, s99, 0xffffff80
	s_or_b32 s99, s99, s63
	s_lshl_b32 s98, s98, 12
	v_lshl_add_u32 v252, v183, 3, s99
	v_lshlrev_b32_e32 v253, 2, v252
	v_lshlrev_b32_e32 v252, 1, v252
	v_lshl_add_u32 v252, v182, 11, v252
	s_add_u32 s100, s10, s98
	s_addc_u32 s101, s11, 0
	global_load_dwordx4 v[234:237], v253, s[100:101]
	global_load_dwordx4 v[242:245], v253, s[100:101] offset:16
	s_add_u32 s100, s8, s98
	s_addc_u32 s101, s9, 0
	global_load_dwordx4 v[238:241], v253, s[100:101]
	global_load_dwordx4 v[246:249], v253, s[100:101] offset:16
	s_lshl_b32 s98, s24, 8
	s_add_i32 s98, s98, s62
	s_lshl_b32 s98, s98, 11
	s_add_u32 s100, s4, s98
	s_addc_u32 s101, s5, 0
	global_load_dwordx4 v[250:253], v252, s[100:101]
	ds_read_b128 v[130:133], v188
	ds_read_b128 v[134:137], v189
	ds_read_b128 v[138:141], v184
	ds_read_b128 v[142:145], v185
	ds_read_b128 v[146:149], v190
	ds_read_b128 v[150:153], v191
	ds_read_b128 v[154:157], v192
	ds_read_b128 v[158:161], v193
	s_add_i32 s75, s28, 0x80
	s_cmp_eq_u32 s66, s80
	s_cselect_b32 s81, s25, s79
	s_cselect_b32 s75, s29, s75
	v_add_u32_e32 v203, s28, v201
	s_add_i32 m0, s46, 0xc000
	ds_read_b128 v[162:165], v202
	ds_read_b128 v[166:169], v202 offset:1024
	ds_read_b128 v[170:173], v202 offset:2048
	ds_read_b128 v[204:207], v202 offset:3072
	ds_read_b128 v[214:217], v202 offset:4096
	ds_read_b128 v[218:221], v202 offset:5120
	ds_read_b128 v[222:225], v202 offset:6144
	ds_read_b128 v[226:229], v202 offset:7168
	global_load_lds_dwordx4 v203, s[4:5]
	v_add_u32_e32 v203, s28, v200
	s_add_i32 m0, s46, 0xe000
	s_nop 0
	global_load_lds_dwordx4 v203, s[4:5]
	s_waitcnt vmcnt(13)
	s_waitcnt lgkmcnt(0)
	s_barrier
	s_setprio 1
	s_waitcnt lgkmcnt(0)
	v_mfma_f32_16x16x32_bf16 v[126:129], v[138:141], v[162:165], 0
	v_mfma_f32_16x16x32_bf16 v[118:121], v[134:137], v[162:165], 0
	v_mfma_f32_16x16x32_bf16 v[110:113], v[138:141], v[170:173], 0
	v_mfma_f32_16x16x32_bf16 v[102:105], v[134:137], v[170:173], 0
	v_mfma_f32_16x16x32_bf16 v[94:97], v[138:141], v[214:217], 0
	v_mfma_f32_16x16x32_bf16 v[86:89], v[134:137], v[214:217], 0
	v_mfma_f32_16x16x32_bf16 v[78:81], v[138:141], v[222:225], 0
	v_mfma_f32_16x16x32_bf16 v[70:73], v[134:137], v[222:225], 0
	v_mfma_f32_16x16x32_bf16 v[126:129], v[130:133], v[166:169], v[126:129]
	v_mfma_f32_16x16x32_bf16 v[118:121], v[146:149], v[166:169], v[118:121]
	v_mfma_f32_16x16x32_bf16 v[110:113], v[130:133], v[204:207], v[110:113]
	v_mfma_f32_16x16x32_bf16 v[102:105], v[146:149], v[204:207], v[102:105]
	v_mfma_f32_16x16x32_bf16 v[94:97], v[130:133], v[218:221], v[94:97]
	v_mfma_f32_16x16x32_bf16 v[86:89], v[146:149], v[218:221], v[86:89]
	v_mfma_f32_16x16x32_bf16 v[78:81], v[130:133], v[226:229], v[78:81]
	v_mfma_f32_16x16x32_bf16 v[70:73], v[146:149], v[226:229], v[70:73]
	s_setprio 0
	s_setprio 1
	v_mfma_f32_16x16x32_bf16 v[122:125], v[142:145], v[162:165], 0
	v_mfma_f32_16x16x32_bf16 v[114:117], v[154:157], v[162:165], 0
	v_mfma_f32_16x16x32_bf16 v[106:109], v[142:145], v[170:173], 0
	v_mfma_f32_16x16x32_bf16 v[98:101], v[154:157], v[170:173], 0
	v_mfma_f32_16x16x32_bf16 v[90:93], v[142:145], v[214:217], 0
	v_mfma_f32_16x16x32_bf16 v[82:85], v[154:157], v[214:217], 0
	v_mfma_f32_16x16x32_bf16 v[74:77], v[142:145], v[222:225], 0
	v_mfma_f32_16x16x32_bf16 v[66:69], v[154:157], v[222:225], 0
	v_mfma_f32_16x16x32_bf16 v[122:125], v[150:153], v[166:169], v[122:125]
	v_mfma_f32_16x16x32_bf16 v[114:117], v[158:161], v[166:169], v[114:117]
	v_mfma_f32_16x16x32_bf16 v[106:109], v[150:153], v[204:207], v[106:109]
	v_mfma_f32_16x16x32_bf16 v[98:101], v[158:161], v[204:207], v[98:101]
	v_mfma_f32_16x16x32_bf16 v[90:93], v[150:153], v[218:221], v[90:93]
	v_mfma_f32_16x16x32_bf16 v[82:85], v[158:161], v[218:221], v[82:85]
	v_mfma_f32_16x16x32_bf16 v[74:77], v[150:153], v[226:229], v[74:77]
	v_mfma_f32_16x16x32_bf16 v[66:69], v[158:161], v[226:229], v[66:69]
	s_setprio 0
	s_barrier
	s_mov_b32 m0, s47
	v_add_u32_e32 v203, s81, v178
	ds_read_b128 v[162:165], v202 offset:16384
	ds_read_b128 v[166:169], v202 offset:17408
	ds_read_b128 v[170:173], v202 offset:18432
	ds_read_b128 v[204:207], v202 offset:19456
	ds_read_b128 v[214:217], v202 offset:20480
	ds_read_b128 v[218:221], v202 offset:21504
	ds_read_b128 v[222:225], v202 offset:22528
	ds_read_b128 v[226:229], v202 offset:23552
	global_load_lds_dwordx4 v203, s[6:7]
	v_add_u32_e32 v203, s35, v203
	s_mov_b32 m0, s48
	s_nop 0
	global_load_lds_dwordx4 v203, s[6:7]
	v_add_u32_e32 v203, s81, v179
	s_mov_b32 m0, s49
	s_nop 0
	global_load_lds_dwordx4 v203, s[6:7]
	v_add_u32_e32 v203, s35, v203
	s_mov_b32 m0, s50
	s_nop 0
	global_load_lds_dwordx4 v203, s[6:7]
	v_add_u32_e32 v203, s75, v1
	s_mov_b32 m0, s46
	s_nop 0
	global_load_lds_dwordx4 v203, s[4:5]
	v_add_u32_e32 v203, s31, v203
	s_mov_b32 m0, s51
	s_nop 0
	global_load_lds_dwordx4 v203, s[4:5]
	s_waitcnt vmcnt(13)
	s_waitcnt lgkmcnt(0)
	s_barrier
	s_setprio 1
	s_waitcnt lgkmcnt(0)
	v_mfma_f32_16x16x32_bf16 v[62:65], v[138:141], v[162:165], 0
	v_mfma_f32_16x16x32_bf16 v[54:57], v[134:137], v[162:165], 0
	v_mfma_f32_16x16x32_bf16 v[46:49], v[138:141], v[170:173], 0
	v_mfma_f32_16x16x32_bf16 v[38:41], v[134:137], v[170:173], 0
	v_mfma_f32_16x16x32_bf16 v[30:33], v[138:141], v[214:217], 0
	v_mfma_f32_16x16x32_bf16 v[22:25], v[134:137], v[214:217], 0
	v_mfma_f32_16x16x32_bf16 v[14:17], v[138:141], v[222:225], 0
	v_mfma_f32_16x16x32_bf16 v[6:9], v[134:137], v[222:225], 0
	v_mfma_f32_16x16x32_bf16 v[62:65], v[130:133], v[166:169], v[62:65]
	v_mfma_f32_16x16x32_bf16 v[54:57], v[146:149], v[166:169], v[54:57]
	v_mfma_f32_16x16x32_bf16 v[46:49], v[130:133], v[204:207], v[46:49]
	v_mfma_f32_16x16x32_bf16 v[38:41], v[146:149], v[204:207], v[38:41]
	v_mfma_f32_16x16x32_bf16 v[30:33], v[130:133], v[218:221], v[30:33]
	v_mfma_f32_16x16x32_bf16 v[22:25], v[146:149], v[218:221], v[22:25]
	v_mfma_f32_16x16x32_bf16 v[14:17], v[130:133], v[226:229], v[14:17]
	v_mfma_f32_16x16x32_bf16 v[6:9], v[146:149], v[226:229], v[6:9]
	s_setprio 0
	s_setprio 1
	v_mfma_f32_16x16x32_bf16 v[58:61], v[142:145], v[162:165], 0
	v_mfma_f32_16x16x32_bf16 v[50:53], v[154:157], v[162:165], 0
	v_mfma_f32_16x16x32_bf16 v[42:45], v[142:145], v[170:173], 0
	v_mfma_f32_16x16x32_bf16 v[34:37], v[154:157], v[170:173], 0
	v_mfma_f32_16x16x32_bf16 v[26:29], v[142:145], v[214:217], 0
	v_mfma_f32_16x16x32_bf16 v[18:21], v[154:157], v[214:217], 0
	v_mfma_f32_16x16x32_bf16 v[10:13], v[142:145], v[222:225], 0
	v_mfma_f32_16x16x32_bf16 v[2:5], v[154:157], v[222:225], 0
	v_mfma_f32_16x16x32_bf16 v[58:61], v[150:153], v[166:169], v[58:61]
	v_mfma_f32_16x16x32_bf16 v[50:53], v[158:161], v[166:169], v[50:53]
	v_mfma_f32_16x16x32_bf16 v[42:45], v[150:153], v[204:207], v[42:45]
	v_mfma_f32_16x16x32_bf16 v[34:37], v[158:161], v[204:207], v[34:37]
	v_mfma_f32_16x16x32_bf16 v[26:29], v[150:153], v[218:221], v[26:29]
	v_mfma_f32_16x16x32_bf16 v[18:21], v[158:161], v[218:221], v[18:21]
	v_mfma_f32_16x16x32_bf16 v[10:13], v[150:153], v[226:229], v[10:13]
	v_mfma_f32_16x16x32_bf16 v[2:5], v[158:161], v[226:229], v[2:5]
	s_setprio 0
	s_barrier
	s_branch .Lmid_3

.LBB0_640:
	s_and_b32 s75, s12, 1
	s_lshl_b32 s12, s12, 6
	s_and_b32 s12, s12, 0xffffff80
	v_mov_b32_e32 v130, v182
	v_mov_b32_e32 v131, v183
	s_or_b32 s12, s12, s63
	s_nop 0
	v_lshl_add_u32 v132, v131, 3, s12
	s_lshl_b32 s12, s75, 12
	s_waitcnt lgkmcnt(0)
	s_add_u32 s28, s10, s12
	s_addc_u32 s29, s11, 0
	s_ashr_i32 s25, s24, 31
	s_lshl_b64 s[24:25], s[24:25], 8
	v_ashrrev_i32_e32 v133, 31, v132
	s_add_u32 s24, s24, s62
	v_lshlrev_b64 v[134:135], 2, v[132:133]
	s_addc_u32 s25, s25, s67
	v_lshl_add_u64 v[136:137], s[28:29], 0, v[134:135]
	s_add_u32 s28, s8, s12
	s_addc_u32 s29, s9, 0
	v_lshl_add_u64 v[134:135], s[28:29], 0, v[134:135]
	v_ashrrev_i32_e32 v131, 31, v130
	v_lshlrev_b64 v[208:209], 1, v[132:133]
	v_lshl_add_u64 v[138:139], s[24:25], 0, v[130:131]
	v_lshl_add_u64 v[132:133], s[4:5], 0, v[208:209]
	v_lshlrev_b64 v[130:131], 11, v[138:139]
	v_lshl_add_u64 v[140:141], v[132:133], 0, v[130:131]
	s_nop 0
	s_mul_i32 s12, s75, 0x8400
	v_lshl_add_u64 v[214:215], v[138:139], 0, s[12:13]
	v_add_co_u32_e32 v138, vcc, s65, v140
	s_nop 1
	v_addc_co_u32_e32 v139, vcc, 0, v141, vcc
	v_add_co_u32_e32 v150, vcc, s54, v140
	s_nop 1
	v_addc_co_u32_e32 v151, vcc, 0, v141, vcc
	v_add_co_u32_e32 v152, vcc, s64, v140
	s_nop 1
	v_addc_co_u32_e32 v153, vcc, 0, v141, vcc
	v_add_co_u32_e32 v154, vcc, s69, v140
	s_nop 1
	v_addc_co_u32_e32 v155, vcc, 0, v141, vcc
	v_add_co_u32_e32 v156, vcc, s70, v140
	s_nop 1
	v_addc_co_u32_e32 v157, vcc, 0, v141, vcc
	v_add_co_u32_e32 v216, vcc, s71, v140
	s_nop 1
	v_addc_co_u32_e32 v217, vcc, 0, v141, vcc
	v_add_co_u32_e32 v140, vcc, s72, v140
	s_nop 1
	v_addc_co_u32_e32 v141, vcc, 0, v141, vcc
	global_load_dwordx4 v[170:173], v[138:139], off
	global_load_dwordx4 v[166:169], v[150:151], off
	global_load_dwordx4 v[162:165], v[152:153], off
	global_load_dwordx4 v[158:161], v[154:155], off
	s_nop 0
	global_load_dwordx4 v[154:157], v[156:157], off
	s_nop 0
	global_load_dwordx4 v[150:153], v[216:217], off
	s_nop 0
	global_load_dwordx4 v[138:141], v[140:141], off
	v_add_f32_e32 v123, v123, v235
	v_mul_f32_e32 v123, 0xbfb8aa3b, v123
	v_add_f32_e32 v127, v127, v239
	v_exp_f32_e32 v123, v123
	v_mul_f32_e32 v127, 0xbfb8aa3b, v127
	v_exp_f32_e32 v127, v127
	v_add_f32_e32 v122, v122, v234
	v_add_f32_e32 v124, v124, v236
	v_mul_f32_e32 v122, 0xbfb8aa3b, v122
	v_add_f32_e32 v126, v126, v238
	v_add_f32_e32 v128, v128, v240
	v_add_f32_e32 v129, v129, v241
	v_add_f32_e32 v123, 1.0, v123
	v_add_f32_e32 v125, v125, v237
	v_mul_f32_e32 v124, 0xbfb8aa3b, v124
	v_exp_f32_e32 v122, v122
	v_mul_f32_e32 v126, 0xbfb8aa3b, v126
	v_mul_f32_e32 v128, 0xbfb8aa3b, v128
	v_rcp_f32_e32 v211, v123
	v_add_f32_e32 v123, 1.0, v127
	v_mul_f32_e32 v127, 0xbfb8aa3b, v129
	v_mul_f32_e32 v125, 0xbfb8aa3b, v125
	v_add_f32_e32 v118, v118, v246
	v_add_f32_e32 v119, v119, v247
	v_exp_f32_e32 v124, v124
	v_exp_f32_e32 v126, v126
	v_exp_f32_e32 v128, v128
	v_exp_f32_e32 v127, v127
	v_exp_f32_e32 v125, v125
	v_mul_f32_e32 v118, 0xbfb8aa3b, v118
	v_mul_f32_e32 v119, 0xbfb8aa3b, v119
	v_exp_f32_e32 v118, v118
	v_exp_f32_e32 v119, v119
	v_add_f32_e32 v122, 1.0, v122
	v_add_f32_e32 v106, v106, v234
	v_add_f32_e32 v124, 1.0, v124
	v_rcp_f32_e32 v203, v122
	v_add_f32_e32 v122, 1.0, v126
	v_add_f32_e32 v126, 1.0, v128
	v_add_f32_e32 v127, 1.0, v127
	v_add_f32_e32 v125, 1.0, v125
	v_mul_f32_e32 v106, 0xbfb8aa3b, v106
	v_add_f32_e32 v111, v111, v239
	v_rcp_f32_e32 v122, v122
	v_rcp_f32_e32 v123, v123
	v_rcp_f32_e32 v126, v126
	v_rcp_f32_e32 v124, v124
	v_rcp_f32_e32 v127, v127
	v_rcp_f32_e32 v125, v125
	v_add_f32_e32 v118, 1.0, v118
	v_add_f32_e32 v119, 1.0, v119
	v_exp_f32_e32 v106, v106
	v_mul_f32_e32 v111, 0xbfb8aa3b, v111
	v_rcp_f32_e32 v118, v118
	v_rcp_f32_e32 v119, v119
	v_exp_f32_e32 v111, v111
	v_lshlrev_b32_e32 v128, 16, v250
	v_and_b32_e32 v129, 0xffff0000, v250
	v_lshlrev_b32_e32 v204, 16, v251
	v_and_b32_e32 v205, 0xffff0000, v251
	v_cvt_pk_bf16_f32 v122, v122, v123
	v_cvt_pk_bf16_f32 v123, v126, v127
	v_mul_f32_e32 v126, v203, v128
	v_mul_f32_e32 v127, v211, v129
	v_mul_f32_e32 v124, v124, v204
	v_mul_f32_e32 v125, v125, v205
	v_add_f32_e32 v106, 1.0, v106
	v_add_f32_e32 v107, v107, v235
	v_cvt_pk_bf16_f32 v126, v126, v127
	v_cvt_pk_bf16_f32 v127, v124, v125
	v_cvt_pk_bf16_f32 v124, v118, v119
	v_mul_f32_e32 v107, 0xbfb8aa3b, v107
	v_rcp_f32_e32 v118, v106
	v_add_f32_e32 v106, 1.0, v111
	v_add_f32_e32 v111, v112, v240
	v_exp_f32_e32 v107, v107
	v_mul_f32_e32 v111, 0xbfb8aa3b, v111
	v_exp_f32_e32 v111, v111
	v_add_f32_e32 v114, v114, v242
	v_add_f32_e32 v115, v115, v243
	v_mul_f32_e32 v114, 0xbfb8aa3b, v114
	v_mul_f32_e32 v115, 0xbfb8aa3b, v115
	v_add_f32_e32 v116, v116, v244
	v_add_f32_e32 v117, v117, v245
	v_add_f32_e32 v107, 1.0, v107
	v_exp_f32_e32 v114, v114
	v_exp_f32_e32 v115, v115
	v_mul_f32_e32 v116, 0xbfb8aa3b, v116
	v_mul_f32_e32 v117, 0xbfb8aa3b, v117
	v_add_f32_e32 v110, v110, v238
	v_rcp_f32_e32 v112, v107
	v_add_f32_e32 v107, 1.0, v111
	v_add_f32_e32 v111, v113, v241
	v_exp_f32_e32 v116, v116
	v_exp_f32_e32 v117, v117
	v_mul_f32_e32 v110, 0xbfb8aa3b, v110
	v_mul_f32_e32 v111, 0xbfb8aa3b, v111
	v_add_f32_e32 v98, v98, v242
	v_add_f32_e32 v99, v99, v243
	v_add_f32_e32 v120, v120, v248
	v_add_f32_e32 v121, v121, v249
	v_exp_f32_e32 v110, v110
	v_exp_f32_e32 v111, v111
	v_mul_f32_e32 v98, 0xbfb8aa3b, v98
	v_mul_f32_e32 v99, 0xbfb8aa3b, v99
	v_add_f32_e32 v100, v100, v244
	v_add_f32_e32 v101, v101, v245
	v_mul_f32_e32 v120, 0xbfb8aa3b, v120
	v_mul_f32_e32 v121, 0xbfb8aa3b, v121
	v_add_f32_e32 v108, v108, v236
	v_add_f32_e32 v109, v109, v237
	v_exp_f32_e32 v98, v98
	v_exp_f32_e32 v99, v99
	v_mul_f32_e32 v100, 0xbfb8aa3b, v100
	v_mul_f32_e32 v101, 0xbfb8aa3b, v101
	v_add_f32_e32 v114, 1.0, v114
	v_add_f32_e32 v115, 1.0, v115
	v_exp_f32_e32 v120, v120
	v_exp_f32_e32 v121, v121
	v_mul_f32_e32 v108, 0xbfb8aa3b, v108
	v_mul_f32_e32 v109, 0xbfb8aa3b, v109
	v_add_f32_e32 v102, v102, v246
	v_add_f32_e32 v103, v103, v247
	v_add_f32_e32 v104, v104, v248
	v_exp_f32_e32 v100, v100
	v_add_f32_e32 v105, v105, v249
	v_exp_f32_e32 v101, v101
	v_rcp_f32_e32 v114, v114
	v_rcp_f32_e32 v115, v115
	v_add_f32_e32 v116, 1.0, v116
	v_add_f32_e32 v117, 1.0, v117
	v_exp_f32_e32 v108, v108
	v_exp_f32_e32 v109, v109
	v_mul_f32_e32 v102, 0xbfb8aa3b, v102
	v_mul_f32_e32 v103, 0xbfb8aa3b, v103
	v_mul_f32_e32 v104, 0xbfb8aa3b, v104
	v_mul_f32_e32 v105, 0xbfb8aa3b, v105
	v_rcp_f32_e32 v116, v116
	v_rcp_f32_e32 v117, v117
	v_add_f32_e32 v110, 1.0, v110
	v_add_f32_e32 v111, 1.0, v111
	v_exp_f32_e32 v102, v102
	v_exp_f32_e32 v103, v103
	v_exp_f32_e32 v104, v104
	v_exp_f32_e32 v105, v105
	v_rcp_f32_e32 v110, v110
	v_rcp_f32_e32 v106, v106
	v_rcp_f32_e32 v107, v107
	v_rcp_f32_e32 v111, v111
	v_add_f32_e32 v98, 1.0, v98
	v_add_f32_e32 v99, 1.0, v99
	v_add_f32_e32 v120, 1.0, v120
	v_add_f32_e32 v121, 1.0, v121
	v_lshlrev_b32_e32 v128, 16, v252
	v_and_b32_e32 v129, 0xffff0000, v252
	v_rcp_f32_e32 v98, v98
	v_rcp_f32_e32 v99, v99
	v_add_f32_e32 v100, 1.0, v100
	v_add_f32_e32 v101, 1.0, v101
	v_rcp_f32_e32 v120, v120
	v_rcp_f32_e32 v121, v121
	v_lshlrev_b32_e32 v203, 16, v253
	v_and_b32_e32 v204, 0xffff0000, v253
	v_mul_f32_e32 v114, v114, v128
	v_mul_f32_e32 v115, v115, v129
	v_add_f32_e32 v108, 1.0, v108
	v_add_f32_e32 v109, 1.0, v109
	v_rcp_f32_e32 v100, v100
	v_rcp_f32_e32 v101, v101
	v_cvt_pk_bf16_f32 v128, v114, v115
	v_mul_f32_e32 v114, v116, v203
	v_mul_f32_e32 v115, v117, v204
	v_rcp_f32_e32 v108, v108
	v_rcp_f32_e32 v109, v109
	s_waitcnt vmcnt(6)
	v_lshlrev_b32_e32 v113, 16, v170
	v_and_b32_e32 v119, 0xffff0000, v170
	v_add_f32_e32 v102, 1.0, v102
	v_add_f32_e32 v103, 1.0, v103
	v_add_f32_e32 v104, 1.0, v104
	v_add_f32_e32 v105, 1.0, v105
	v_cvt_pk_bf16_f32 v129, v114, v115
	v_lshlrev_b64 v[114:115], 11, v[214:215]
	v_cvt_pk_bf16_f32 v106, v110, v106
	v_cvt_pk_bf16_f32 v107, v107, v111
	v_mul_f32_e32 v110, v118, v113
	v_mul_f32_e32 v111, v112, v119
	v_rcp_f32_e32 v102, v102
	v_rcp_f32_e32 v103, v103
	v_rcp_f32_e32 v104, v104
	v_rcp_f32_e32 v105, v105
	v_lshlrev_b32_e32 v112, 16, v172
	v_and_b32_e32 v113, 0xffff0000, v172
	v_add_f32_e32 v90, v90, v234
	v_lshl_add_u64 v[116:117], s[16:17], 0, v[114:115]
	v_lshlrev_b32_e32 v118, 16, v173
	v_and_b32_e32 v119, 0xffff0000, v173
	v_mul_f32_e32 v98, v98, v112
	v_mul_f32_e32 v99, v99, v113
	v_mul_f32_e32 v90, 0xbfb8aa3b, v90
	v_add_f32_e32 v95, v95, v239
	v_cvt_pk_bf16_f32 v125, v120, v121
	v_lshl_add_u64 v[116:117], v[116:117], 0, v[208:209]
	v_lshl_add_u64 v[114:115], s[18:19], 0, v[114:115]
	v_lshlrev_b32_e32 v120, 16, v171
	v_and_b32_e32 v121, 0xffff0000, v171
	v_cvt_pk_bf16_f32 v112, v98, v99
	v_mul_f32_e32 v98, v100, v118
	v_mul_f32_e32 v99, v101, v119
	v_exp_f32_e32 v90, v90
	v_mul_f32_e32 v95, 0xbfb8aa3b, v95
	v_lshl_add_u64 v[114:115], v[114:115], 0, v[208:209]
	v_mul_f32_e32 v108, v108, v120
	v_mul_f32_e32 v109, v109, v121
	v_cvt_pk_bf16_f32 v113, v98, v99
	v_add_co_u32_e32 v98, vcc, s65, v116
	v_exp_f32_e32 v95, v95
	global_store_dwordx4 v[116:117], v[122:125], off
	global_store_dwordx4 v[114:115], v[126:129], off
	v_cvt_pk_bf16_f32 v110, v110, v111
	v_cvt_pk_bf16_f32 v111, v108, v109
	v_cvt_pk_bf16_f32 v108, v102, v103
	v_cvt_pk_bf16_f32 v109, v104, v105
	v_addc_co_u32_e32 v99, vcc, 0, v117, vcc
	global_store_dwordx4 v[98:99], v[106:109], off
	v_add_co_u32_e32 v98, vcc, s65, v114
	v_add_f32_e32 v90, 1.0, v90
	s_nop 0
	v_addc_co_u32_e32 v99, vcc, 0, v115, vcc
	v_add_f32_e32 v91, v91, v235
	global_store_dwordx4 v[98:99], v[110:113], off
	v_mul_f32_e32 v91, 0xbfb8aa3b, v91
	v_rcp_f32_e32 v98, v90
	v_add_f32_e32 v90, 1.0, v95
	v_add_f32_e32 v95, v96, v240
	v_exp_f32_e32 v91, v91
	v_mul_f32_e32 v95, 0xbfb8aa3b, v95
	v_exp_f32_e32 v95, v95
	v_add_f32_e32 v94, v94, v238
	v_add_f32_e32 v91, 1.0, v91
	v_rcp_f32_e32 v96, v91
	v_add_f32_e32 v91, 1.0, v95
	v_add_f32_e32 v95, v97, v241
	v_mul_f32_e32 v94, 0xbfb8aa3b, v94
	v_mul_f32_e32 v95, 0xbfb8aa3b, v95
	v_add_f32_e32 v82, v82, v242
	v_add_f32_e32 v83, v83, v243
	v_exp_f32_e32 v94, v94
	v_exp_f32_e32 v95, v95
	v_mul_f32_e32 v82, 0xbfb8aa3b, v82
	v_mul_f32_e32 v83, 0xbfb8aa3b, v83
	v_add_f32_e32 v84, v84, v244
	v_add_f32_e32 v85, v85, v245
	v_add_f32_e32 v92, v92, v236
	v_add_f32_e32 v93, v93, v237
	v_exp_f32_e32 v82, v82
	v_exp_f32_e32 v83, v83
	v_mul_f32_e32 v84, 0xbfb8aa3b, v84
	v_mul_f32_e32 v85, 0xbfb8aa3b, v85
	v_mul_f32_e32 v92, 0xbfb8aa3b, v92
	v_mul_f32_e32 v93, 0xbfb8aa3b, v93
	v_add_f32_e32 v86, v86, v246
	v_add_f32_e32 v87, v87, v247
	v_add_f32_e32 v88, v88, v248
	v_exp_f32_e32 v84, v84
	v_add_f32_e32 v89, v89, v249
	v_exp_f32_e32 v85, v85
	v_exp_f32_e32 v92, v92
	v_exp_f32_e32 v93, v93
	v_mul_f32_e32 v86, 0xbfb8aa3b, v86
	v_mul_f32_e32 v87, 0xbfb8aa3b, v87
	v_mul_f32_e32 v88, 0xbfb8aa3b, v88
	v_mul_f32_e32 v89, 0xbfb8aa3b, v89
	v_add_f32_e32 v94, 1.0, v94
	v_add_f32_e32 v95, 1.0, v95
	v_exp_f32_e32 v86, v86
	v_exp_f32_e32 v87, v87
	v_exp_f32_e32 v88, v88
	v_exp_f32_e32 v89, v89
	v_rcp_f32_e32 v94, v94
	v_rcp_f32_e32 v90, v90
	v_rcp_f32_e32 v91, v91
	v_rcp_f32_e32 v95, v95
	v_add_f32_e32 v82, 1.0, v82
	v_add_f32_e32 v83, 1.0, v83
	v_rcp_f32_e32 v82, v82
	v_rcp_f32_e32 v83, v83
	v_add_f32_e32 v84, 1.0, v84
	v_add_f32_e32 v85, 1.0, v85
	v_add_f32_e32 v92, 1.0, v92
	v_add_f32_e32 v93, 1.0, v93
	v_rcp_f32_e32 v84, v84
	v_rcp_f32_e32 v85, v85
	v_rcp_f32_e32 v92, v92
	v_rcp_f32_e32 v93, v93
	s_waitcnt vmcnt(9)
	v_lshlrev_b32_e32 v97, 16, v166
	v_and_b32_e32 v99, 0xffff0000, v166
	v_add_f32_e32 v86, 1.0, v86
	v_add_f32_e32 v87, 1.0, v87
	v_add_f32_e32 v88, 1.0, v88
	v_add_f32_e32 v89, 1.0, v89
	v_cvt_pk_bf16_f32 v90, v94, v90
	v_cvt_pk_bf16_f32 v91, v91, v95
	v_mul_f32_e32 v94, v98, v97
	v_mul_f32_e32 v95, v96, v99
	v_rcp_f32_e32 v86, v86
	v_rcp_f32_e32 v87, v87
	v_rcp_f32_e32 v88, v88
	v_rcp_f32_e32 v89, v89
	v_lshlrev_b32_e32 v96, 16, v168
	v_and_b32_e32 v97, 0xffff0000, v168
	v_add_f32_e32 v74, v74, v234
	v_lshlrev_b32_e32 v98, 16, v169
	v_and_b32_e32 v99, 0xffff0000, v169
	v_mul_f32_e32 v82, v82, v96
	v_mul_f32_e32 v83, v83, v97
	v_mul_f32_e32 v74, 0xbfb8aa3b, v74
	v_add_f32_e32 v79, v79, v239
	v_lshlrev_b32_e32 v100, 16, v167
	v_and_b32_e32 v101, 0xffff0000, v167
	v_cvt_pk_bf16_f32 v96, v82, v83
	v_mul_f32_e32 v82, v84, v98
	v_mul_f32_e32 v83, v85, v99
	v_exp_f32_e32 v74, v74
	v_mul_f32_e32 v79, 0xbfb8aa3b, v79
	v_mul_f32_e32 v92, v92, v100
	v_mul_f32_e32 v93, v93, v101
	v_cvt_pk_bf16_f32 v97, v82, v83
	v_add_co_u32_e32 v82, vcc, s54, v116
	v_exp_f32_e32 v79, v79
	v_cvt_pk_bf16_f32 v94, v94, v95
	v_cvt_pk_bf16_f32 v95, v92, v93
	v_cvt_pk_bf16_f32 v92, v86, v87
	v_cvt_pk_bf16_f32 v93, v88, v89
	v_addc_co_u32_e32 v83, vcc, 0, v117, vcc
	global_store_dwordx4 v[82:83], v[90:93], off
	v_add_co_u32_e32 v82, vcc, s54, v114
	v_add_f32_e32 v74, 1.0, v74
	s_nop 0
	v_addc_co_u32_e32 v83, vcc, 0, v115, vcc
	v_add_f32_e32 v75, v75, v235
	global_store_dwordx4 v[82:83], v[94:97], off
	v_mul_f32_e32 v75, 0xbfb8aa3b, v75
	v_rcp_f32_e32 v82, v74
	v_add_f32_e32 v74, 1.0, v79
	v_add_f32_e32 v79, v80, v240
	v_exp_f32_e32 v75, v75
	v_mul_f32_e32 v79, 0xbfb8aa3b, v79
	v_exp_f32_e32 v79, v79
	v_add_f32_e32 v78, v78, v238
	v_add_f32_e32 v75, 1.0, v75
	v_rcp_f32_e32 v80, v75
	v_add_f32_e32 v75, 1.0, v79
	v_add_f32_e32 v79, v81, v241
	v_mul_f32_e32 v78, 0xbfb8aa3b, v78
	v_mul_f32_e32 v79, 0xbfb8aa3b, v79
	v_add_f32_e32 v66, v66, v242
	v_add_f32_e32 v67, v67, v243
	v_exp_f32_e32 v78, v78
	v_exp_f32_e32 v79, v79
	v_mul_f32_e32 v66, 0xbfb8aa3b, v66
	v_mul_f32_e32 v67, 0xbfb8aa3b, v67
	v_add_f32_e32 v68, v68, v244
	v_add_f32_e32 v69, v69, v245
	v_add_f32_e32 v76, v76, v236
	v_add_f32_e32 v77, v77, v237
	v_exp_f32_e32 v66, v66
	v_exp_f32_e32 v67, v67
	v_mul_f32_e32 v68, 0xbfb8aa3b, v68
	v_mul_f32_e32 v69, 0xbfb8aa3b, v69
	v_mul_f32_e32 v76, 0xbfb8aa3b, v76
	v_mul_f32_e32 v77, 0xbfb8aa3b, v77
	v_add_f32_e32 v70, v70, v246
	v_add_f32_e32 v71, v71, v247
	v_add_f32_e32 v72, v72, v248
	v_exp_f32_e32 v68, v68
	v_add_f32_e32 v73, v73, v249
	v_exp_f32_e32 v69, v69
	v_exp_f32_e32 v76, v76
	v_exp_f32_e32 v77, v77
	v_mul_f32_e32 v70, 0xbfb8aa3b, v70
	v_mul_f32_e32 v71, 0xbfb8aa3b, v71
	v_mul_f32_e32 v72, 0xbfb8aa3b, v72
	v_mul_f32_e32 v73, 0xbfb8aa3b, v73
	v_add_f32_e32 v78, 1.0, v78
	v_add_f32_e32 v79, 1.0, v79
	v_exp_f32_e32 v70, v70
	v_exp_f32_e32 v71, v71
	v_exp_f32_e32 v72, v72
	v_exp_f32_e32 v73, v73
	v_rcp_f32_e32 v78, v78
	v_rcp_f32_e32 v74, v74
	v_rcp_f32_e32 v75, v75
	v_rcp_f32_e32 v79, v79
	v_add_f32_e32 v66, 1.0, v66
	v_add_f32_e32 v67, 1.0, v67
	v_rcp_f32_e32 v66, v66
	v_rcp_f32_e32 v67, v67
	v_add_f32_e32 v68, 1.0, v68
	v_add_f32_e32 v69, 1.0, v69
	v_add_f32_e32 v76, 1.0, v76
	v_add_f32_e32 v77, 1.0, v77
	v_rcp_f32_e32 v68, v68
	v_rcp_f32_e32 v69, v69
	v_rcp_f32_e32 v76, v76
	v_rcp_f32_e32 v77, v77
	s_waitcnt vmcnt(10)
	v_lshlrev_b32_e32 v81, 16, v162
	v_and_b32_e32 v83, 0xffff0000, v162
	v_add_f32_e32 v70, 1.0, v70
	v_add_f32_e32 v71, 1.0, v71
	v_add_f32_e32 v72, 1.0, v72
	v_add_f32_e32 v73, 1.0, v73
	v_cvt_pk_bf16_f32 v74, v78, v74
	v_cvt_pk_bf16_f32 v75, v75, v79
	v_mul_f32_e32 v78, v82, v81
	v_mul_f32_e32 v79, v80, v83
	v_rcp_f32_e32 v70, v70
	v_rcp_f32_e32 v71, v71
	v_rcp_f32_e32 v72, v72
	v_rcp_f32_e32 v73, v73
	v_lshlrev_b32_e32 v80, 16, v164
	v_and_b32_e32 v81, 0xffff0000, v164
	v_add_f32_e32 v58, v58, v234
	v_lshlrev_b32_e32 v82, 16, v165
	v_and_b32_e32 v83, 0xffff0000, v165
	v_mul_f32_e32 v66, v66, v80
	v_mul_f32_e32 v67, v67, v81
	v_mul_f32_e32 v58, 0xbfb8aa3b, v58
	v_add_f32_e32 v63, v63, v239
	v_lshlrev_b32_e32 v84, 16, v163
	v_and_b32_e32 v85, 0xffff0000, v163
	v_cvt_pk_bf16_f32 v80, v66, v67
	v_mul_f32_e32 v66, v68, v82
	v_mul_f32_e32 v67, v69, v83
	v_exp_f32_e32 v58, v58
	v_mul_f32_e32 v63, 0xbfb8aa3b, v63
	v_mul_f32_e32 v76, v76, v84
	v_mul_f32_e32 v77, v77, v85
	v_cvt_pk_bf16_f32 v81, v66, v67
	v_add_co_u32_e32 v66, vcc, s64, v116
	v_exp_f32_e32 v63, v63
	v_cvt_pk_bf16_f32 v78, v78, v79
	v_cvt_pk_bf16_f32 v79, v76, v77
	v_cvt_pk_bf16_f32 v76, v70, v71
	v_cvt_pk_bf16_f32 v77, v72, v73
	v_addc_co_u32_e32 v67, vcc, 0, v117, vcc
	global_store_dwordx4 v[66:67], v[74:77], off
	v_add_co_u32_e32 v66, vcc, s64, v114
	v_add_f32_e32 v58, 1.0, v58
	s_nop 0
	v_addc_co_u32_e32 v67, vcc, 0, v115, vcc
	v_add_f32_e32 v59, v59, v235
	global_store_dwordx4 v[66:67], v[78:81], off
	v_mul_f32_e32 v59, 0xbfb8aa3b, v59
	v_rcp_f32_e32 v66, v58
	v_add_f32_e32 v58, 1.0, v63
	v_add_f32_e32 v63, v64, v240
	v_exp_f32_e32 v59, v59
	v_mul_f32_e32 v63, 0xbfb8aa3b, v63
	v_exp_f32_e32 v63, v63
	v_add_f32_e32 v62, v62, v238
	v_add_f32_e32 v59, 1.0, v59
	v_rcp_f32_e32 v64, v59
	v_add_f32_e32 v59, 1.0, v63
	v_add_f32_e32 v63, v65, v241
	v_mul_f32_e32 v62, 0xbfb8aa3b, v62
	v_mul_f32_e32 v63, 0xbfb8aa3b, v63
	v_add_f32_e32 v50, v50, v242
	v_add_f32_e32 v51, v51, v243
	v_exp_f32_e32 v62, v62
	v_exp_f32_e32 v63, v63
	v_mul_f32_e32 v50, 0xbfb8aa3b, v50
	v_mul_f32_e32 v51, 0xbfb8aa3b, v51
	v_add_f32_e32 v52, v52, v244
	v_add_f32_e32 v53, v53, v245
	v_add_f32_e32 v60, v60, v236
	v_add_f32_e32 v61, v61, v237
	v_exp_f32_e32 v50, v50
	v_exp_f32_e32 v51, v51
	v_mul_f32_e32 v52, 0xbfb8aa3b, v52
	v_mul_f32_e32 v53, 0xbfb8aa3b, v53
	v_mul_f32_e32 v60, 0xbfb8aa3b, v60
	v_mul_f32_e32 v61, 0xbfb8aa3b, v61
	v_add_f32_e32 v54, v54, v246
	v_add_f32_e32 v55, v55, v247
	v_add_f32_e32 v56, v56, v248
	v_exp_f32_e32 v52, v52
	v_add_f32_e32 v57, v57, v249
	v_exp_f32_e32 v53, v53
	v_exp_f32_e32 v60, v60
	v_exp_f32_e32 v61, v61
	v_mul_f32_e32 v54, 0xbfb8aa3b, v54
	v_mul_f32_e32 v55, 0xbfb8aa3b, v55
	v_mul_f32_e32 v56, 0xbfb8aa3b, v56
	v_mul_f32_e32 v57, 0xbfb8aa3b, v57
	v_add_f32_e32 v62, 1.0, v62
	v_add_f32_e32 v63, 1.0, v63
	v_exp_f32_e32 v54, v54
	v_exp_f32_e32 v55, v55
	v_exp_f32_e32 v56, v56
	v_exp_f32_e32 v57, v57
	v_rcp_f32_e32 v62, v62
	v_rcp_f32_e32 v58, v58
	v_rcp_f32_e32 v59, v59
	v_rcp_f32_e32 v63, v63
	v_add_f32_e32 v50, 1.0, v50
	v_add_f32_e32 v51, 1.0, v51
	v_rcp_f32_e32 v50, v50
	v_rcp_f32_e32 v51, v51
	v_add_f32_e32 v52, 1.0, v52
	v_add_f32_e32 v53, 1.0, v53
	v_add_f32_e32 v60, 1.0, v60
	v_add_f32_e32 v61, 1.0, v61
	v_rcp_f32_e32 v52, v52
	v_rcp_f32_e32 v53, v53
	v_rcp_f32_e32 v60, v60
	v_rcp_f32_e32 v61, v61
	s_waitcnt vmcnt(11)
	v_lshlrev_b32_e32 v65, 16, v158
	v_and_b32_e32 v67, 0xffff0000, v158
	v_add_f32_e32 v54, 1.0, v54
	v_add_f32_e32 v55, 1.0, v55
	v_add_f32_e32 v56, 1.0, v56
	v_add_f32_e32 v57, 1.0, v57
	v_cvt_pk_bf16_f32 v58, v62, v58
	v_cvt_pk_bf16_f32 v59, v59, v63
	v_mul_f32_e32 v62, v66, v65
	v_mul_f32_e32 v63, v64, v67
	v_rcp_f32_e32 v54, v54
	v_rcp_f32_e32 v55, v55
	v_rcp_f32_e32 v56, v56
	v_rcp_f32_e32 v57, v57
	v_lshlrev_b32_e32 v64, 16, v160
	v_and_b32_e32 v65, 0xffff0000, v160
	v_add_f32_e32 v42, v42, v234
	v_lshlrev_b32_e32 v66, 16, v161
	v_and_b32_e32 v67, 0xffff0000, v161
	v_mul_f32_e32 v50, v50, v64
	v_mul_f32_e32 v51, v51, v65
	v_mul_f32_e32 v42, 0xbfb8aa3b, v42
	v_add_f32_e32 v47, v47, v239
	v_lshlrev_b32_e32 v68, 16, v159
	v_and_b32_e32 v69, 0xffff0000, v159
	v_cvt_pk_bf16_f32 v64, v50, v51
	v_mul_f32_e32 v50, v52, v66
	v_mul_f32_e32 v51, v53, v67
	v_exp_f32_e32 v42, v42
	v_mul_f32_e32 v47, 0xbfb8aa3b, v47
	v_mul_f32_e32 v60, v60, v68
	v_mul_f32_e32 v61, v61, v69
	v_cvt_pk_bf16_f32 v65, v50, v51
	v_add_co_u32_e32 v50, vcc, s69, v116
	v_exp_f32_e32 v47, v47
	v_cvt_pk_bf16_f32 v62, v62, v63
	v_cvt_pk_bf16_f32 v63, v60, v61
	v_cvt_pk_bf16_f32 v60, v54, v55
	v_cvt_pk_bf16_f32 v61, v56, v57
	v_addc_co_u32_e32 v51, vcc, 0, v117, vcc
	global_store_dwordx4 v[50:51], v[58:61], off
	v_add_co_u32_e32 v50, vcc, s69, v114
	v_add_f32_e32 v42, 1.0, v42
	s_nop 0
	v_addc_co_u32_e32 v51, vcc, 0, v115, vcc
	v_add_f32_e32 v43, v43, v235
	global_store_dwordx4 v[50:51], v[62:65], off
	v_mul_f32_e32 v43, 0xbfb8aa3b, v43
	v_rcp_f32_e32 v50, v42
	v_add_f32_e32 v42, 1.0, v47
	v_add_f32_e32 v47, v48, v240
	v_exp_f32_e32 v43, v43
	v_mul_f32_e32 v47, 0xbfb8aa3b, v47
	v_exp_f32_e32 v47, v47
	v_add_f32_e32 v46, v46, v238
	v_add_f32_e32 v43, 1.0, v43
	v_rcp_f32_e32 v48, v43
	v_add_f32_e32 v43, 1.0, v47
	v_add_f32_e32 v47, v49, v241
	v_mul_f32_e32 v46, 0xbfb8aa3b, v46
	v_mul_f32_e32 v47, 0xbfb8aa3b, v47
	v_add_f32_e32 v34, v34, v242
	v_add_f32_e32 v35, v35, v243
	v_exp_f32_e32 v46, v46
	v_exp_f32_e32 v47, v47
	v_mul_f32_e32 v34, 0xbfb8aa3b, v34
	v_mul_f32_e32 v35, 0xbfb8aa3b, v35
	v_add_f32_e32 v36, v36, v244
	v_add_f32_e32 v37, v37, v245
	v_add_f32_e32 v44, v44, v236
	v_add_f32_e32 v45, v45, v237
	v_exp_f32_e32 v34, v34
	v_exp_f32_e32 v35, v35
	v_mul_f32_e32 v36, 0xbfb8aa3b, v36
	v_mul_f32_e32 v37, 0xbfb8aa3b, v37
	v_mul_f32_e32 v44, 0xbfb8aa3b, v44
	v_mul_f32_e32 v45, 0xbfb8aa3b, v45
	v_add_f32_e32 v38, v38, v246
	v_add_f32_e32 v39, v39, v247
	v_add_f32_e32 v40, v40, v248
	v_exp_f32_e32 v36, v36
	v_add_f32_e32 v41, v41, v249
	v_exp_f32_e32 v37, v37
	v_exp_f32_e32 v44, v44
	v_exp_f32_e32 v45, v45
	v_mul_f32_e32 v38, 0xbfb8aa3b, v38
	v_mul_f32_e32 v39, 0xbfb8aa3b, v39
	v_mul_f32_e32 v40, 0xbfb8aa3b, v40
	v_mul_f32_e32 v41, 0xbfb8aa3b, v41
	v_add_f32_e32 v46, 1.0, v46
	v_add_f32_e32 v47, 1.0, v47
	v_exp_f32_e32 v38, v38
	v_exp_f32_e32 v39, v39
	v_exp_f32_e32 v40, v40
	v_exp_f32_e32 v41, v41
	v_rcp_f32_e32 v46, v46
	v_rcp_f32_e32 v42, v42
	v_rcp_f32_e32 v43, v43
	v_rcp_f32_e32 v47, v47
	v_add_f32_e32 v34, 1.0, v34
	v_add_f32_e32 v35, 1.0, v35
	v_rcp_f32_e32 v34, v34
	v_rcp_f32_e32 v35, v35
	v_add_f32_e32 v36, 1.0, v36
	v_add_f32_e32 v37, 1.0, v37
	v_add_f32_e32 v44, 1.0, v44
	v_add_f32_e32 v45, 1.0, v45
	v_rcp_f32_e32 v36, v36
	v_rcp_f32_e32 v37, v37
	v_rcp_f32_e32 v44, v44
	v_rcp_f32_e32 v45, v45
	s_waitcnt vmcnt(12)
	v_lshlrev_b32_e32 v49, 16, v154
	v_and_b32_e32 v51, 0xffff0000, v154
	v_add_f32_e32 v38, 1.0, v38
	v_add_f32_e32 v39, 1.0, v39
	v_add_f32_e32 v40, 1.0, v40
	v_add_f32_e32 v41, 1.0, v41
	v_cvt_pk_bf16_f32 v42, v46, v42
	v_cvt_pk_bf16_f32 v43, v43, v47
	v_mul_f32_e32 v46, v50, v49
	v_mul_f32_e32 v47, v48, v51
	v_rcp_f32_e32 v38, v38
	v_rcp_f32_e32 v39, v39
	v_rcp_f32_e32 v40, v40
	v_rcp_f32_e32 v41, v41
	v_lshlrev_b32_e32 v48, 16, v156
	v_and_b32_e32 v49, 0xffff0000, v156
	v_add_f32_e32 v26, v26, v234
	v_lshlrev_b32_e32 v50, 16, v157
	v_and_b32_e32 v51, 0xffff0000, v157
	v_mul_f32_e32 v34, v34, v48
	v_mul_f32_e32 v35, v35, v49
	v_mul_f32_e32 v26, 0xbfb8aa3b, v26
	v_add_f32_e32 v31, v31, v239
	v_lshlrev_b32_e32 v52, 16, v155
	v_and_b32_e32 v53, 0xffff0000, v155
	v_cvt_pk_bf16_f32 v48, v34, v35
	v_mul_f32_e32 v34, v36, v50
	v_mul_f32_e32 v35, v37, v51
	v_exp_f32_e32 v26, v26
	v_mul_f32_e32 v31, 0xbfb8aa3b, v31
	v_mul_f32_e32 v44, v44, v52
	v_mul_f32_e32 v45, v45, v53
	v_cvt_pk_bf16_f32 v49, v34, v35
	v_add_co_u32_e32 v34, vcc, s70, v116
	v_exp_f32_e32 v31, v31
	v_cvt_pk_bf16_f32 v46, v46, v47
	v_cvt_pk_bf16_f32 v47, v44, v45
	v_cvt_pk_bf16_f32 v44, v38, v39
	v_cvt_pk_bf16_f32 v45, v40, v41
	v_addc_co_u32_e32 v35, vcc, 0, v117, vcc
	global_store_dwordx4 v[34:35], v[42:45], off
	v_add_co_u32_e32 v34, vcc, s70, v114
	v_add_f32_e32 v26, 1.0, v26
	s_nop 0
	v_addc_co_u32_e32 v35, vcc, 0, v115, vcc
	v_add_f32_e32 v27, v27, v235
	global_store_dwordx4 v[34:35], v[46:49], off
	v_mul_f32_e32 v27, 0xbfb8aa3b, v27
	v_rcp_f32_e32 v34, v26
	v_add_f32_e32 v26, 1.0, v31
	v_add_f32_e32 v31, v32, v240
	v_exp_f32_e32 v27, v27
	v_mul_f32_e32 v31, 0xbfb8aa3b, v31
	v_exp_f32_e32 v31, v31
	v_add_f32_e32 v30, v30, v238
	v_add_f32_e32 v27, 1.0, v27
	v_rcp_f32_e32 v32, v27
	v_add_f32_e32 v27, 1.0, v31
	v_add_f32_e32 v31, v33, v241
	v_mul_f32_e32 v30, 0xbfb8aa3b, v30
	v_mul_f32_e32 v31, 0xbfb8aa3b, v31
	v_add_f32_e32 v18, v18, v242
	v_add_f32_e32 v19, v19, v243
	v_exp_f32_e32 v30, v30
	v_exp_f32_e32 v31, v31
	v_mul_f32_e32 v18, 0xbfb8aa3b, v18
	v_mul_f32_e32 v19, 0xbfb8aa3b, v19
	v_add_f32_e32 v20, v20, v244
	v_add_f32_e32 v21, v21, v245
	v_add_f32_e32 v28, v28, v236
	v_add_f32_e32 v29, v29, v237
	v_exp_f32_e32 v18, v18
	v_exp_f32_e32 v19, v19
	v_mul_f32_e32 v20, 0xbfb8aa3b, v20
	v_mul_f32_e32 v21, 0xbfb8aa3b, v21
	v_mul_f32_e32 v28, 0xbfb8aa3b, v28
	v_mul_f32_e32 v29, 0xbfb8aa3b, v29
	v_add_f32_e32 v22, v22, v246
	v_add_f32_e32 v23, v23, v247
	v_add_f32_e32 v24, v24, v248
	v_exp_f32_e32 v20, v20
	v_add_f32_e32 v25, v25, v249
	v_exp_f32_e32 v21, v21
	v_exp_f32_e32 v28, v28
	v_exp_f32_e32 v29, v29
	v_mul_f32_e32 v22, 0xbfb8aa3b, v22
	v_mul_f32_e32 v23, 0xbfb8aa3b, v23
	v_mul_f32_e32 v24, 0xbfb8aa3b, v24
	v_mul_f32_e32 v25, 0xbfb8aa3b, v25
	v_add_f32_e32 v30, 1.0, v30
	v_add_f32_e32 v31, 1.0, v31
	v_exp_f32_e32 v22, v22
	v_exp_f32_e32 v23, v23
	v_exp_f32_e32 v24, v24
	v_exp_f32_e32 v25, v25
	v_rcp_f32_e32 v30, v30
	v_rcp_f32_e32 v26, v26
	v_rcp_f32_e32 v27, v27
	v_rcp_f32_e32 v31, v31
	v_add_f32_e32 v18, 1.0, v18
	v_add_f32_e32 v19, 1.0, v19
	v_rcp_f32_e32 v18, v18
	v_rcp_f32_e32 v19, v19
	v_add_f32_e32 v20, 1.0, v20
	v_add_f32_e32 v21, 1.0, v21
	v_add_f32_e32 v28, 1.0, v28
	v_add_f32_e32 v29, 1.0, v29
	v_rcp_f32_e32 v20, v20
	v_rcp_f32_e32 v21, v21
	v_rcp_f32_e32 v28, v28
	v_rcp_f32_e32 v29, v29
	s_waitcnt vmcnt(13)
	v_lshlrev_b32_e32 v33, 16, v150
	v_and_b32_e32 v35, 0xffff0000, v150
	v_add_f32_e32 v22, 1.0, v22
	v_add_f32_e32 v23, 1.0, v23
	v_add_f32_e32 v24, 1.0, v24
	v_add_f32_e32 v25, 1.0, v25
	v_cvt_pk_bf16_f32 v26, v30, v26
	v_cvt_pk_bf16_f32 v27, v27, v31
	v_mul_f32_e32 v30, v34, v33
	v_mul_f32_e32 v31, v32, v35
	v_rcp_f32_e32 v22, v22
	v_rcp_f32_e32 v23, v23
	v_rcp_f32_e32 v24, v24
	v_rcp_f32_e32 v25, v25
	v_lshlrev_b32_e32 v32, 16, v152
	v_and_b32_e32 v33, 0xffff0000, v152
	v_add_f32_e32 v10, v10, v234
	v_lshlrev_b32_e32 v34, 16, v153
	v_and_b32_e32 v35, 0xffff0000, v153
	v_mul_f32_e32 v18, v18, v32
	v_mul_f32_e32 v19, v19, v33
	v_mul_f32_e32 v10, 0xbfb8aa3b, v10
	v_add_f32_e32 v15, v15, v239
	v_lshlrev_b32_e32 v36, 16, v151
	v_and_b32_e32 v37, 0xffff0000, v151
	v_cvt_pk_bf16_f32 v32, v18, v19
	v_mul_f32_e32 v18, v20, v34
	v_mul_f32_e32 v19, v21, v35
	v_exp_f32_e32 v10, v10
	v_mul_f32_e32 v15, 0xbfb8aa3b, v15
	v_mul_f32_e32 v28, v28, v36
	v_mul_f32_e32 v29, v29, v37
	v_cvt_pk_bf16_f32 v33, v18, v19
	v_add_co_u32_e32 v18, vcc, s71, v116
	v_exp_f32_e32 v15, v15
	v_cvt_pk_bf16_f32 v30, v30, v31
	v_cvt_pk_bf16_f32 v31, v28, v29
	v_cvt_pk_bf16_f32 v28, v22, v23
	v_cvt_pk_bf16_f32 v29, v24, v25
	v_addc_co_u32_e32 v19, vcc, 0, v117, vcc
	global_store_dwordx4 v[18:19], v[26:29], off
	v_add_co_u32_e32 v18, vcc, s71, v114
	v_add_f32_e32 v10, 1.0, v10
	s_nop 0
	v_addc_co_u32_e32 v19, vcc, 0, v115, vcc
	v_add_f32_e32 v11, v11, v235
	global_store_dwordx4 v[18:19], v[30:33], off
	v_mul_f32_e32 v11, 0xbfb8aa3b, v11
	v_rcp_f32_e32 v18, v10
	v_add_f32_e32 v10, 1.0, v15
	v_add_f32_e32 v15, v16, v240
	v_exp_f32_e32 v11, v11
	v_mul_f32_e32 v15, 0xbfb8aa3b, v15
	v_exp_f32_e32 v15, v15
	v_add_f32_e32 v14, v14, v238
	v_add_f32_e32 v11, 1.0, v11
	v_rcp_f32_e32 v16, v11
	v_add_f32_e32 v11, 1.0, v15
	v_add_f32_e32 v15, v17, v241
	v_mul_f32_e32 v14, 0xbfb8aa3b, v14
	v_mul_f32_e32 v15, 0xbfb8aa3b, v15
	v_add_f32_e32 v2, v2, v242
	v_add_f32_e32 v3, v3, v243
	v_exp_f32_e32 v14, v14
	v_exp_f32_e32 v15, v15
	v_mul_f32_e32 v2, 0xbfb8aa3b, v2
	v_mul_f32_e32 v3, 0xbfb8aa3b, v3
	v_add_f32_e32 v4, v4, v244
	v_add_f32_e32 v5, v5, v245
	v_add_f32_e32 v12, v12, v236
	v_add_f32_e32 v13, v13, v237
	v_exp_f32_e32 v2, v2
	v_exp_f32_e32 v3, v3
	v_mul_f32_e32 v4, 0xbfb8aa3b, v4
	v_mul_f32_e32 v5, 0xbfb8aa3b, v5
	v_mul_f32_e32 v12, 0xbfb8aa3b, v12
	v_mul_f32_e32 v13, 0xbfb8aa3b, v13
	v_add_f32_e32 v6, v6, v246
	v_add_f32_e32 v7, v7, v247
	v_add_f32_e32 v8, v8, v248
	v_exp_f32_e32 v4, v4
	v_add_f32_e32 v9, v9, v249
	v_exp_f32_e32 v5, v5
	v_exp_f32_e32 v12, v12
	v_exp_f32_e32 v13, v13
	v_mul_f32_e32 v6, 0xbfb8aa3b, v6
	v_mul_f32_e32 v7, 0xbfb8aa3b, v7
	v_mul_f32_e32 v8, 0xbfb8aa3b, v8
	v_mul_f32_e32 v9, 0xbfb8aa3b, v9
	v_add_f32_e32 v14, 1.0, v14
	v_add_f32_e32 v15, 1.0, v15
	v_exp_f32_e32 v6, v6
	v_exp_f32_e32 v7, v7
	v_exp_f32_e32 v8, v8
	v_exp_f32_e32 v9, v9
	v_rcp_f32_e32 v14, v14
	v_rcp_f32_e32 v10, v10
	v_rcp_f32_e32 v11, v11
	v_rcp_f32_e32 v15, v15
	v_add_f32_e32 v2, 1.0, v2
	v_add_f32_e32 v3, 1.0, v3
	v_rcp_f32_e32 v2, v2
	v_rcp_f32_e32 v3, v3
	v_add_f32_e32 v4, 1.0, v4
	v_add_f32_e32 v5, 1.0, v5
	v_add_f32_e32 v12, 1.0, v12
	v_add_f32_e32 v13, 1.0, v13
	v_rcp_f32_e32 v4, v4
	v_rcp_f32_e32 v5, v5
	v_rcp_f32_e32 v12, v12
	v_rcp_f32_e32 v13, v13
	s_waitcnt vmcnt(14)
	v_lshlrev_b32_e32 v17, 16, v138
	v_and_b32_e32 v19, 0xffff0000, v138
	v_add_f32_e32 v6, 1.0, v6
	v_add_f32_e32 v7, 1.0, v7
	v_add_f32_e32 v8, 1.0, v8
	v_add_f32_e32 v9, 1.0, v9
	v_cvt_pk_bf16_f32 v10, v14, v10
	v_cvt_pk_bf16_f32 v11, v11, v15
	v_mul_f32_e32 v14, v18, v17
	v_mul_f32_e32 v15, v16, v19
	v_rcp_f32_e32 v6, v6
	v_rcp_f32_e32 v7, v7
	v_rcp_f32_e32 v8, v8
	v_rcp_f32_e32 v9, v9
	v_lshlrev_b32_e32 v16, 16, v140
	v_and_b32_e32 v17, 0xffff0000, v140
	v_lshlrev_b32_e32 v18, 16, v141
	v_and_b32_e32 v19, 0xffff0000, v141
	v_mul_f32_e32 v2, v2, v16
	v_mul_f32_e32 v3, v3, v17
	v_lshlrev_b32_e32 v20, 16, v139
	v_and_b32_e32 v21, 0xffff0000, v139
	v_cvt_pk_bf16_f32 v16, v2, v3
	v_mul_f32_e32 v2, v4, v18
	v_mul_f32_e32 v3, v5, v19
	v_mul_f32_e32 v12, v12, v20
	v_mul_f32_e32 v13, v13, v21
	v_cvt_pk_bf16_f32 v17, v2, v3
	v_add_co_u32_e32 v2, vcc, 0x58000, v116
	v_cvt_pk_bf16_f32 v14, v14, v15
	v_cvt_pk_bf16_f32 v15, v12, v13
	v_cvt_pk_bf16_f32 v12, v6, v7
	v_cvt_pk_bf16_f32 v13, v8, v9
	v_addc_co_u32_e32 v3, vcc, 0, v117, vcc
	global_store_dwordx4 v[2:3], v[10:13], off
	v_add_co_u32_e32 v2, vcc, 0x58000, v114
	s_nop 1
	v_addc_co_u32_e32 v3, vcc, 0, v115, vcc
	global_store_dwordx4 v[2:3], v[14:17], off
	s_andn2_b64 vcc, exec, s[2:3]
	s_mov_b64 s[2:3], -1
	s_cbranch_vccnz .LBB0_632
	s_andn2_b64 vcc, exec, s[14:15]
	s_cbranch_vccnz .LBB0_631
	s_barrier
	s_branch .LBB0_631
